# speedup vs baseline: 1.0568x; 1.0039x over previous
.LBB0_102:
	v_sub_f32_e32 v105, v105, v5
	v_sub_f32_e32 v104, v104, v5
	v_exp_f32_e32 v105, v105
	v_exp_f32_e32 v104, v104
	v_sub_f32_e32 v103, v107, v5
	ds_write2_b64 v92, v[66:67], v[68:69] offset1:4
	ds_write2_b64 v92, v[62:63], v[64:65] offset0:8 offset1:12
	ds_read_b64_tr_b16 v[62:63], v93
	ds_read_b64_tr_b16 v[64:65], v93 offset:32
	v_cndmask_b32_e64 v107, v105, 0, s[40:41]
	v_cndmask_b32_e64 v108, v104, 0, s[44:45]
	ds_read_b64_tr_b16 v[68:69], v93 offset:64
	ds_read_b64_tr_b16 v[104:105], v93 offset:96
	ds_write2_b64 v92, v[58:59], v[60:61] offset1:4
	ds_write2_b64 v92, v[54:55], v[56:57] offset0:8 offset1:12
	ds_read_b64_tr_b16 v[54:55], v93
	v_sub_f32_e32 v106, v106, v5
	v_exp_f32_e32 v103, v103
	v_exp_f32_e32 v106, v106
	ds_read_b64_tr_b16 v[56:57], v93 offset:32
	ds_read_b64_tr_b16 v[58:59], v93 offset:64
	ds_read_b64_tr_b16 v[60:61], v93 offset:96
	v_cndmask_b32_e64 v103, v103, 0, s[46:47]
	v_cndmask_b32_e64 v106, v106, 0, s[42:43]
	v_cvt_pk_f16_f32 v67, v106, v108
	v_cvt_pk_f16_f32 v66, v103, v107
	s_waitcnt lgkmcnt(3)
	s_cmp_eq_u32 s81, 0
	s_cbranch_scc1 .Lattn_g_first
	v_mfma_f32_16x16x16_f16 v[30:33], v[54:55], v[66:67], v[30:33]
	v_add_f32_e32 v54, 0, v103
	v_add_f32_e32 v54, v107, v54
	v_add_f32_e32 v54, v106, v54
	v_mfma_f32_16x16x16_f16 v[46:49], v[62:63], v[66:67], v[46:49]
	v_add_f32_e32 v54, v108, v54
	v_fmac_f32_e32 v54, v4, v2
	v_mfma_f32_16x16x16_f16 v[50:53], v[64:65], v[66:67], v[50:53]
	v_mfma_f32_16x16x16_f16 v[38:41], v[68:69], v[66:67], v[38:41]
	v_mfma_f32_16x16x16_f16 v[42:45], v[104:105], v[66:67], v[42:45]
	s_waitcnt lgkmcnt(2)
	v_mfma_f32_16x16x16_f16 v[34:37], v[56:57], v[66:67], v[34:37]
	s_waitcnt lgkmcnt(1)
	v_mfma_f32_16x16x16_f16 v[22:25], v[58:59], v[66:67], v[22:25]
	s_waitcnt lgkmcnt(0)
	v_mfma_f32_16x16x16_f16 v[26:29], v[60:61], v[66:67], v[26:29]
	s_branch .Lattn_g_done
.Lattn_g_first:
	v_mfma_f32_16x16x16_f16 v[30:33], v[54:55], v[66:67], 0
	v_add_f32_e32 v54, 0, v103
	v_add_f32_e32 v54, v107, v54
	v_add_f32_e32 v54, v106, v54
	v_mfma_f32_16x16x16_f16 v[46:49], v[62:63], v[66:67], 0
	v_add_f32_e32 v54, v108, v54
	v_fmac_f32_e32 v54, v4, v2
	v_mfma_f32_16x16x16_f16 v[50:53], v[64:65], v[66:67], 0
	v_mfma_f32_16x16x16_f16 v[38:41], v[68:69], v[66:67], 0
	v_mfma_f32_16x16x16_f16 v[42:45], v[104:105], v[66:67], 0
	s_waitcnt lgkmcnt(2)
	v_mfma_f32_16x16x16_f16 v[34:37], v[56:57], v[66:67], 0
	s_waitcnt lgkmcnt(1)
	v_mfma_f32_16x16x16_f16 v[22:25], v[58:59], v[66:67], 0
	s_waitcnt lgkmcnt(0)
	v_mfma_f32_16x16x16_f16 v[26:29], v[60:61], v[66:67], 0
.Lattn_g_done:
	s_and_saveexec_b64 s[40:41], s[0:1]
	s_cbranch_execz .LBB0_108
	ds_bpermute_b32 v2, v90, v54
	s_waitcnt vmcnt(5)
	v_mov_b32_e32 v99, v112
	v_mov_b32_e32 v100, v113
	v_mov_b32_e32 v101, v114
	v_mov_b32_e32 v102, v115
	s_waitcnt lgkmcnt(0)
	v_add_f32_e32 v54, v54, v2
	ds_bpermute_b32 v55, v91, v54
	s_lshl_b32 s95, s80, 1
	v_mov_b32_e32 v2, s95
	v_or_b32_e32 v4, 1, v2
	v_cmp_gt_i32_e32 vcc, s33, v4
	ds_read_b128 v[4:7], v86 offset:32768
	ds_read_b128 v[8:11], v86 offset:33792
	ds_read_b128 v[12:15], v86 offset:34816
	ds_read_b128 v[16:19], v86 offset:35840
	v_cvt_pk_f16_f32 v53, v52, v53
	v_cvt_pk_f16_f32 v52, v50, v51
	v_cvt_pk_f16_f32 v51, v48, v49
	v_cvt_pk_f16_f32 v50, v46, v47
	v_cvt_pk_f16_f32 v45, v44, v45
	v_cvt_pk_f16_f32 v44, v42, v43
	v_cvt_pk_f16_f32 v43, v40, v41
	v_cvt_pk_f16_f32 v42, v38, v39
	v_cvt_pk_f16_f32 v37, v36, v37
	v_cvt_pk_f16_f32 v36, v34, v35
	v_cvt_pk_f16_f32 v35, v32, v33
	v_cvt_pk_f16_f32 v34, v30, v31
	ds_read_b128 v[30:33], v86 offset:36864
	ds_read_b128 v[38:41], v86 offset:37888
	ds_read_b128 v[46:49], v86 offset:38912
	ds_read_b128 v[56:59], v86 offset:39936
	v_cvt_pk_f16_f32 v63, v28, v29
	v_cvt_pk_f16_f32 v62, v26, v27
	v_cvt_pk_f16_f32 v61, v24, v25
	v_cvt_pk_f16_f32 v60, v22, v23
	s_waitcnt lgkmcnt(7)
	v_mfma_f32_16x16x32_f16 v[4:7], v[4:7], v[50:53], 0
	s_waitcnt lgkmcnt(6)
	v_mfma_f32_16x16x32_f16 v[4:7], v[8:11], v[42:45], v[4:7]
	s_waitcnt lgkmcnt(5)
	v_mfma_f32_16x16x32_f16 v[4:7], v[12:15], v[34:37], v[4:7]
	s_waitcnt lgkmcnt(4)
	v_mfma_f32_16x16x32_f16 v[12:15], v[16:19], v[60:63], v[4:7]
	ds_read_b128 v[8:11], v86 offset:44032
	ds_read_b128 v[16:19], v86 offset:43008
	ds_read_b128 v[20:23], v86 offset:41984
	ds_read_b128 v[24:27], v86 offset:40960
	s_waitcnt lgkmcnt(7)
	v_mfma_f32_16x16x32_f16 v[4:7], v[30:33], v[50:53], 0
	s_waitcnt lgkmcnt(6)
	v_mfma_f32_16x16x32_f16 v[4:7], v[38:41], v[42:45], v[4:7]
	s_waitcnt lgkmcnt(5)
	v_mfma_f32_16x16x32_f16 v[4:7], v[46:49], v[34:37], v[4:7]
	s_waitcnt lgkmcnt(4)
	v_mfma_f32_16x16x32_f16 v[4:7], v[56:59], v[60:63], v[4:7]
	ds_read_b128 v[28:31], v86 offset:45056
	ds_read_b128 v[38:41], v86 offset:46080
	ds_read_b128 v[46:49], v86 offset:47104
	ds_read_b128 v[56:59], v86 offset:48128
	s_waitcnt lgkmcnt(4)
	v_mfma_f32_16x16x32_f16 v[24:27], v[24:27], v[50:53], 0
	v_mfma_f32_16x16x32_f16 v[20:23], v[20:23], v[42:45], v[24:27]
	v_mfma_f32_16x16x32_f16 v[16:19], v[16:19], v[34:37], v[20:23]
	v_mfma_f32_16x16x32_f16 v[8:11], v[8:11], v[60:63], v[16:19]
	s_nop 5
	ds_read_b128 v[20:23], v86 offset:52224
	ds_read_b128 v[24:27], v86 offset:51200
	ds_read_b128 v[64:67], v86 offset:50176
	ds_read_b128 v[104:107], v86 offset:49152
	s_waitcnt lgkmcnt(7)
	v_mfma_f32_16x16x32_f16 v[16:19], v[28:31], v[50:53], 0
	s_waitcnt lgkmcnt(6)
	v_mfma_f32_16x16x32_f16 v[16:19], v[38:41], v[42:45], v[16:19]
	s_waitcnt lgkmcnt(5)
	v_mfma_f32_16x16x32_f16 v[16:19], v[46:49], v[34:37], v[16:19]
	s_waitcnt lgkmcnt(4)
	v_mfma_f32_16x16x32_f16 v[16:19], v[56:59], v[60:63], v[16:19]
	ds_read_b128 v[28:31], v86 offset:53248
	ds_read_b128 v[38:41], v86 offset:54272
	ds_read_b128 v[46:49], v86 offset:55296
	ds_read_b128 v[56:59], v86 offset:56320
	s_waitcnt lgkmcnt(4)
	v_mfma_f32_16x16x32_f16 v[104:107], v[104:107], v[50:53], 0
	v_mfma_f32_16x16x32_f16 v[64:67], v[64:67], v[42:45], v[104:107]
	v_mfma_f32_16x16x32_f16 v[24:27], v[24:27], v[34:37], v[64:67]
	v_mfma_f32_16x16x32_f16 v[20:23], v[20:23], v[60:63], v[24:27]
	s_nop 5
	ds_read_b128 v[64:67], v86 offset:60416
	ds_read_b128 v[104:107], v86 offset:59392
	ds_read_b128 v[108:111], v86 offset:58368
	ds_read_b128 v[112:115], v86 offset:57344
	s_waitcnt lgkmcnt(7)
	v_mfma_f32_16x16x32_f16 v[24:27], v[28:31], v[50:53], 0
	s_waitcnt lgkmcnt(6)
	v_mfma_f32_16x16x32_f16 v[24:27], v[38:41], v[42:45], v[24:27]
	s_waitcnt lgkmcnt(5)
	v_mfma_f32_16x16x32_f16 v[24:27], v[46:49], v[34:37], v[24:27]
	s_waitcnt lgkmcnt(4)
	v_mfma_f32_16x16x32_f16 v[24:27], v[56:59], v[60:63], v[24:27]
	ds_read_b128 v[38:41], v86 offset:61440
	ds_read_b128 v[46:49], v86 offset:62464
	ds_read_b128 v[56:59], v86 offset:63488
	ds_read_b128 v[116:119], v86 offset:64512
	s_waitcnt lgkmcnt(4)
	v_mfma_f32_16x16x32_f16 v[28:31], v[112:115], v[50:53], 0
	v_mfma_f32_16x16x32_f16 v[28:31], v[108:111], v[42:45], v[28:31]
	v_mfma_f32_16x16x32_f16 v[28:31], v[104:107], v[34:37], v[28:31]
	v_mfma_f32_16x16x32_f16 v[28:31], v[64:67], v[60:63], v[28:31]
	s_waitcnt lgkmcnt(3)
	v_mfma_f32_16x16x32_f16 v[38:41], v[38:41], v[50:53], 0
	s_waitcnt lgkmcnt(2)
	v_mfma_f32_16x16x32_f16 v[38:41], v[46:49], v[42:45], v[38:41]
	s_waitcnt lgkmcnt(1)
	v_mfma_f32_16x16x32_f16 v[32:35], v[56:59], v[34:37], v[38:41]
	s_waitcnt lgkmcnt(0)
	v_mfma_f32_16x16x32_f16 v[32:35], v[116:119], v[60:63], v[32:35]
	s_or_b64 s[42:43], s[38:39], vcc
	s_and_saveexec_b64 s[0:1], s[42:43]
	s_cbranch_execz .LBB0_105
	v_lshlrev_b32_e32 v36, 1, v78
	ds_read_b128 v[36:39], v36 offset:27472
	v_cndmask_b32_e64 v12, 0, v12, s[14:15]
	v_cndmask_b32_e64 v13, 0, v13, s[14:15]
	v_cndmask_b32_e64 v14, 0, v14, s[14:15]
	v_cndmask_b32_e64 v15, 0, v15, s[14:15]
	v_cndmask_b32_e64 v7, v15, v7, s[12:13]
	v_cndmask_b32_e64 v6, v14, v6, s[12:13]
	v_cndmask_b32_e64 v5, v13, v5, s[12:13]
	v_cndmask_b32_e64 v4, v12, v4, s[12:13]
	v_add_f32_e32 v40, v54, v55
	v_cndmask_b32_e64 v4, v4, v8, s[10:11]
	v_cndmask_b32_e64 v5, v5, v9, s[10:11]
	v_cndmask_b32_e64 v6, v6, v10, s[10:11]
	v_cndmask_b32_e64 v7, v7, v11, s[10:11]
	v_rcp_f32_e32 v12, v40
	v_cndmask_b32_e64 v7, v7, v19, s[8:9]
	v_cndmask_b32_e64 v6, v6, v18, s[8:9]
	v_cndmask_b32_e64 v5, v5, v17, s[8:9]
	v_cndmask_b32_e64 v4, v4, v16, s[8:9]
	v_cndmask_b32_e64 v4, v4, v20, s[6:7]
	v_cndmask_b32_e64 v5, v5, v21, s[6:7]
	v_cndmask_b32_e64 v6, v6, v22, s[6:7]
	v_cndmask_b32_e64 v7, v7, v23, s[6:7]
	v_cndmask_b32_e64 v7, v7, v27, s[20:21]
	v_cndmask_b32_e64 v6, v6, v26, s[20:21]
	v_cndmask_b32_e64 v5, v5, v25, s[20:21]
	v_cndmask_b32_e64 v4, v4, v24, s[20:21]
	v_cmp_lt_f32_e32 vcc, 0, v40
	v_cndmask_b32_e64 v4, v4, v28, s[18:19]
	v_cndmask_b32_e64 v5, v5, v29, s[18:19]
	v_cndmask_b32_e64 v6, v6, v30, s[18:19]
	v_cndmask_b32_e64 v7, v7, v31, s[18:19]
	v_cndmask_b32_e32 v8, 0, v12, vcc
	v_cndmask_b32_e64 v7, v7, v35, s[16:17]
	v_cndmask_b32_e64 v6, v6, v34, s[16:17]
	v_cndmask_b32_e64 v5, v5, v33, s[16:17]
	v_cndmask_b32_e64 v4, v4, v32, s[16:17]
	v_or_b32_e32 v2, v2, v89
	s_waitcnt lgkmcnt(0)
	v_fma_mixlo_f16 v4, v8, v4, v36
	v_fma_mixlo_f16 v5, v8, v5, v37
	v_fma_mixlo_f16 v6, v8, v6, v38
	v_fma_mixlo_f16 v7, v8, v7, v39
	v_cndmask_b32_e32 v4, 0, v4, vcc
	v_cndmask_b32_e32 v8, 0, v5, vcc
	v_cndmask_b32_e32 v5, 0, v6, vcc
	v_cndmask_b32_e32 v6, 0, v7, vcc
	v_pack_b32_f16 v5, v5, v6
	v_pack_b32_f16 v4, v4, v8
	v_mad_u64_u32 v[6:7], s[42:43], v2, s72, v[78:79]
	ds_write_b64 v6, v[4:5]
.LBB0_105:
	s_or_b64 exec, exec, s[0:1]
	s_and_saveexec_b64 s[0:1], s[78:79]
	s_cbranch_execz .LBB0_107
	ds_read_b128 v[4:7], v86
	ds_read_b128 v[8:11], v86 offset:1024
	ds_read_b128 v[12:15], v86 offset:4096
	ds_read_b128 v[22:25], v86 offset:5120
	ds_read_b128 v[34:37], v86 offset:2048
	ds_read_b128 v[38:41], v86 offset:3072
	ds_read_b128 v[42:45], v86 offset:6144
	ds_read_b128 v[46:49], v86 offset:7168
	v_cndmask_b32_e64 v21, 0, v102, s[22:23]
	v_cndmask_b32_e64 v20, 0, v101, s[22:23]
	v_cndmask_b32_e64 v19, 0, v100, s[22:23]
	v_cndmask_b32_e64 v18, 0, v99, s[22:23]
	v_cndmask_b32_e64 v29, 0, v102, s[24:25]
	v_cndmask_b32_e64 v28, 0, v101, s[24:25]
	v_cndmask_b32_e64 v27, 0, v100, s[24:25]
	v_cndmask_b32_e64 v26, 0, v99, s[24:25]
	v_cndmask_b32_e64 v33, 0, v102, s[26:27]
	v_cndmask_b32_e64 v32, 0, v101, s[26:27]
	v_cndmask_b32_e64 v31, 0, v100, s[26:27]
	v_cndmask_b32_e64 v30, 0, v99, s[26:27]
	v_cndmask_b32_e64 v53, 0, v102, s[28:29]
	v_cndmask_b32_e64 v52, 0, v101, s[28:29]
	v_cndmask_b32_e64 v51, 0, v100, s[28:29]
	v_cndmask_b32_e64 v50, 0, v99, s[28:29]
	s_waitcnt lgkmcnt(7)
	v_mfma_f32_16x16x32_f16 v[4:7], v[4:7], v[18:21], 0
	s_waitcnt lgkmcnt(5)
	v_mfma_f32_16x16x32_f16 v[12:15], v[12:15], v[18:21], 0
	v_mfma_f32_16x16x32_f16 v[4:7], v[8:11], v[26:29], v[4:7]
	s_waitcnt lgkmcnt(4)
	v_mfma_f32_16x16x32_f16 v[8:11], v[22:25], v[26:29], v[12:15]
	s_nop 4
	ds_read_b128 v[12:15], v86 offset:13312
	ds_read_b128 v[22:25], v86 offset:12288
	ds_read_b128 v[54:57], v86 offset:9216
	ds_read_b128 v[58:61], v86 offset:8192
	s_waitcnt lgkmcnt(7)
	v_mfma_f32_16x16x32_f16 v[4:7], v[34:37], v[30:33], v[4:7]
	s_waitcnt lgkmcnt(5)
	v_mfma_f32_16x16x32_f16 v[8:11], v[42:45], v[30:33], v[8:11]
	s_waitcnt lgkmcnt(4)
	v_mfma_f32_16x16x32_f16 v[34:37], v[46:49], v[50:53], v[8:11]
	v_mfma_f32_16x16x32_f16 v[4:7], v[38:41], v[50:53], v[4:7]
	s_nop 6
	v_cvt_pk_f16_f32 v9, v36, v37
	v_cvt_pk_f16_f32 v8, v34, v35
	v_cvt_pk_f16_f32 v7, v6, v7
	v_cvt_pk_f16_f32 v6, v4, v5
	ds_read_b128 v[34:37], v86 offset:10240
	ds_read_b128 v[38:41], v86 offset:11264
	ds_read_b128 v[42:45], v86 offset:14336
	ds_read_b128 v[46:49], v86 offset:15360
	s_waitcnt lgkmcnt(6)
	v_mfma_f32_16x16x32_f16 v[22:25], v[22:25], v[18:21], 0
	s_waitcnt lgkmcnt(4)
	v_mfma_f32_16x16x32_f16 v[58:61], v[58:61], v[18:21], 0
	v_mfma_f32_16x16x32_f16 v[10:13], v[12:15], v[26:29], v[22:25]
	v_mfma_f32_16x16x32_f16 v[54:57], v[54:57], v[26:29], v[58:61]
	ds_read_b128 v[14:17], v86 offset:21504
	s_nop 2
	ds_read_b128 v[22:25], v86 offset:20480
	s_nop 0
	ds_read_b128 v[58:61], v86 offset:17408
	ds_read_b128 v[62:65], v86 offset:16384
	s_waitcnt lgkmcnt(7)
	v_mfma_f32_16x16x32_f16 v[34:37], v[34:37], v[30:33], v[54:57]
	s_waitcnt lgkmcnt(5)
	v_mfma_f32_16x16x32_f16 v[10:13], v[42:45], v[30:33], v[10:13]
	s_waitcnt lgkmcnt(4)
	v_mfma_f32_16x16x32_f16 v[10:13], v[46:49], v[50:53], v[10:13]
	v_mfma_f32_16x16x32_f16 v[34:37], v[38:41], v[50:53], v[34:37]
	s_nop 6
	v_cvt_pk_f16_f32 v13, v12, v13
	v_cvt_pk_f16_f32 v12, v10, v11
	v_cvt_pk_f16_f32 v11, v36, v37
	v_cvt_pk_f16_f32 v10, v34, v35
	ds_read_b128 v[34:37], v86 offset:18432
	ds_read_b128 v[38:41], v86 offset:19456
	ds_read_b128 v[42:45], v86 offset:22528
	ds_read_b128 v[46:49], v86 offset:23552
	s_waitcnt lgkmcnt(6)
	v_mfma_f32_16x16x32_f16 v[22:25], v[22:25], v[18:21], 0
	s_waitcnt lgkmcnt(4)
	v_mfma_f32_16x16x32_f16 v[54:57], v[62:65], v[18:21], 0
	v_mfma_f32_16x16x32_f16 v[14:17], v[14:17], v[26:29], v[22:25]
	v_mfma_f32_16x16x32_f16 v[54:57], v[58:61], v[26:29], v[54:57]
	s_nop 3
	ds_read_b128 v[22:25], v86 offset:29696
	ds_read_b128 v[58:61], v86 offset:28672
	ds_read_b128 v[62:65], v86 offset:25600
	ds_read_b128 v[66:69], v86 offset:24576
	s_waitcnt lgkmcnt(7)
	v_mfma_f32_16x16x32_f16 v[34:37], v[34:37], v[30:33], v[54:57]
	s_waitcnt lgkmcnt(5)
	v_mfma_f32_16x16x32_f16 v[14:17], v[42:45], v[30:33], v[14:17]
	s_waitcnt lgkmcnt(4)
	v_mfma_f32_16x16x32_f16 v[14:17], v[46:49], v[50:53], v[14:17]
	v_mfma_f32_16x16x32_f16 v[34:37], v[38:41], v[50:53], v[34:37]
	s_nop 6
	v_cvt_pk_f16_f32 v17, v16, v17
	v_cvt_pk_f16_f32 v16, v14, v15
	v_cvt_pk_f16_f32 v15, v36, v37
	v_cvt_pk_f16_f32 v14, v34, v35
	ds_read_b128 v[34:37], v86 offset:26624
	ds_read_b128 v[38:41], v86 offset:27648
	ds_read_b128 v[42:45], v86 offset:30720
	ds_read_b128 v[46:49], v86 offset:31744
	s_waitcnt lgkmcnt(4)
	v_mfma_f32_16x16x32_f16 v[54:57], v[66:69], v[18:21], 0
	v_mfma_f32_16x16x32_f16 v[18:21], v[58:61], v[18:21], 0
	v_mfma_f32_16x16x32_f16 v[18:21], v[22:25], v[26:29], v[18:21]
	v_mfma_f32_16x16x32_f16 v[54:57], v[62:65], v[26:29], v[54:57]
	s_waitcnt lgkmcnt(3)
	v_mfma_f32_16x16x32_f16 v[22:25], v[34:37], v[30:33], v[54:57]
	s_waitcnt lgkmcnt(1)
	v_mfma_f32_16x16x32_f16 v[18:21], v[42:45], v[30:33], v[18:21]
	s_waitcnt lgkmcnt(0)
	v_mfma_f32_16x16x32_f16 v[18:21], v[46:49], v[50:53], v[18:21]
	v_mfma_f32_16x16x32_f16 v[22:25], v[38:41], v[50:53], v[22:25]
	s_nop 6
	v_cvt_pk_f16_f32 v21, v20, v21
	v_cvt_pk_f16_f32 v20, v18, v19
	v_cvt_pk_f16_f32 v19, v24, v25
	v_cvt_pk_f16_f32 v18, v22, v23
.LBB0_107:
	s_or_b64 exec, exec, s[0:1]
	v_mov_b32_e32 v5, 0xf149f2ca
	v_mov_b32_e32 v54, 0

.LBB0_118:
	s_or_b64 exec, exec, s[60:61]
	v_lshrrev_b32_e32 v42, 8, v0
	v_lshlrev_b32_e32 v50, 4, v42
	v_bfe_u32 v36, v0, 6, 2
	v_lshl_or_b32 v44, v36, 13, v86
	v_mov_b32_e32 v45, 0
	v_lshl_add_u64 v[18:19], s[56:57], 0, v[44:45]
	v_add_co_u32_e32 v34, vcc, 0x1000, v18
	global_load_dwordx4 v[2:5], v44, s[56:57]
	global_load_dwordx4 v[6:9], v44, s[56:57] offset:1024
	global_load_dwordx4 v[10:13], v44, s[56:57] offset:2048
	global_load_dwordx4 v[14:17], v44, s[56:57] offset:3072
	v_addc_co_u32_e32 v35, vcc, 0, v19, vcc
	v_lshlrev_b32_e32 v44, 7, v36
	global_load_dwordx4 v[18:21], v[34:35], off
	global_load_dwordx4 v[22:25], v[34:35], off offset:1024
	global_load_dwordx4 v[26:29], v[34:35], off offset:2048
	global_load_dwordx4 v[30:33], v[34:35], off offset:3072
	v_lshl_add_u64 v[34:35], s[52:53], 0, v[44:45]
	v_lshlrev_b32_e32 v36, 2, v1
	v_mov_b32_e32 v37, v45
	v_lshl_add_u64 v[46:47], v[34:35], 0, v[36:37]
	global_load_dwordx4 v[34:37], v[46:47], off offset:16
	global_load_dwordx4 v[38:41], v[46:47], off
	v_add3_u32 v46, s66, v50, v79
	v_ashrrev_i32_e32 v47, 31, v46
	v_and_b32_e32 v0, 48, v0
	v_lshlrev_b64 v[46:47], 9, v[46:47]
	v_lshlrev_b32_e32 v0, 1, v0
	v_or3_b32 v46, v46, v44, v0
	v_mul_u32_u24_e32 v43, 0x110, v79
	s_movk_i32 s0, 0x1100
	v_lshl_add_u64 v[0:1], s[54:55], 0, v[46:47]
	v_mad_u32_u24 v42, v42, s0, v43
	s_mov_b32 s0, 0x10000
	v_lshl_add_u64 v[0:1], v[0:1], 0, 16
	v_add3_u32 v51, v42, v70, s0
	v_cmp_gt_i32_e32 vcc, s33, v50
	s_waitcnt lgkmcnt(0)
	s_barrier
	s_and_saveexec_b64 s[0:1], vcc
	s_cbranch_execz .LBB0_123
	s_mov_b64 s[0:1], 0
	s_mov_b64 s[2:3], 0x8000
	s_waitcnt vmcnt(0)
	s_branch .LBB0_121
